# speedup vs baseline: 1.0048x; 1.0048x over previous
_Z11gemm_kernelILi1ELi1EEvPKDF16_S1_iiPKfS3_S3_PDF16_S4_S4_Pf:
	s_load_dwordx4 s[4:7], s[0:1], 0x0
	s_load_dwordx2 s[8:9], s[0:1], 0x48
	s_load_dwordx2 s[10:11], s[0:1], 0x18
	v_readfirstlane_b32 s12, v0
	v_and_b32_e32 v1, 63, v0
	s_lshr_b32 s12, s12, 6
	s_lshr_b32 s13, s12, 1
	s_and_b32 s14, s12, 1
	s_and_b32 s15, s2, 7
	s_lshr_b32 s16, s2, 3
	s_lshr_b32 s17, s16, 4
	s_lshl_b32 s15, s15, 2
	s_add_i32 s15, s15, s17
	s_and_b32 s16, s16, 15
	v_lshrrev_b32_e32 v2, 3, v1
	v_and_b32_e32 v3, 7, v1
	v_lshrrev_b32_e32 v4, 1, v2
	v_xor_b32_e32 v3, v3, v4
	v_lshlrev_b32_e32 v3, 4, v3
	v_lshl_or_b32 v2, v2, 11, v3
	v_xor_b32_e32 v3, 64, v2
	v_add_u32_e32 v3, 0x4000, v3
	v_add_u32_e32 v4, 0x8000, v2
	v_add_u32_e32 v5, 0x8000, v3
	v_and_b32_e32 v14, 31, v1
	v_lshlrev_b32_e32 v14, 2, v14
	s_lshl_b32 s20, s12, 12
	s_lshl_b32 s21, s12, 11
	s_add_i32 s21, s21, 0xc000
	s_lshl_b32 s22, s16, 8
	s_lshl_b32 s23, s14, 7
	s_add_i32 s22, s22, s23
	s_waitcnt lgkmcnt(0)
	s_add_u32 s10, s10, s22
	s_addc_u32 s11, s11, 0
	global_load_dword v14, v14, s[10:11]
	s_lshl_b32 s23, s15, 18
	s_lshl_b32 s24, s12, 16
	s_add_i32 s23, s23, s24
	s_add_u32 s4, s4, s23
	s_addc_u32 s5, s5, 0
	s_lshl_b32 s23, s16, 17
	s_lshl_b32 s24, s12, 15
	s_add_i32 s23, s23, s24
	s_add_u32 s6, s6, s23
	s_addc_u32 s7, s7, 0
	s_lshl_b32 s23, s15, 19
	s_lshl_b32 s24, s13, 18
	s_add_i32 s23, s23, s24
	s_add_i32 s23, s23, s22
	s_add_u32 s8, s8, s23
	s_addc_u32 s9, s9, 0
	s_add_u32 m0, s20, 0x0
	s_nop 0
	global_load_lds_dwordx4 v2, s[4:5]
	s_add_u32 m0, s20, 0x400
	s_nop 0
	global_load_lds_dwordx4 v3, s[4:5]
	s_add_u32 m0, s20, 0x800
	s_nop 0
	global_load_lds_dwordx4 v4, s[4:5]
	s_add_u32 m0, s20, 0xc00
	s_nop 0
	global_load_lds_dwordx4 v5, s[4:5]
	s_add_u32 m0, s21, 0x0
	s_nop 0
	global_load_lds_dwordx4 v2, s[6:7]
	s_add_u32 m0, s21, 0x400
	s_nop 0
	global_load_lds_dwordx4 v3, s[6:7]
	s_add_u32 s4, s4, 0x80
	s_addc_u32 s5, s5, 0
	s_add_u32 s6, s6, 0x80
	s_addc_u32 s7, s7, 0
	s_add_u32 m0, s20, 0x4000
	s_nop 0
	global_load_lds_dwordx4 v2, s[4:5]
	s_add_u32 m0, s20, 0x4400
	s_nop 0
	global_load_lds_dwordx4 v3, s[4:5]
	s_add_u32 m0, s20, 0x4800
	s_nop 0
	global_load_lds_dwordx4 v4, s[4:5]
	s_add_u32 m0, s20, 0x4c00
	s_nop 0
	global_load_lds_dwordx4 v5, s[4:5]
	s_add_u32 m0, s21, 0x2000
	s_nop 0
	global_load_lds_dwordx4 v2, s[6:7]
	s_add_u32 m0, s21, 0x2400
	s_nop 0
	global_load_lds_dwordx4 v3, s[6:7]
	s_add_u32 s4, s4, 0x80
	s_addc_u32 s5, s5, 0
	s_add_u32 s6, s6, 0x80
	s_addc_u32 s7, s7, 0
	v_and_b32_e32 v48, 31, v1
	v_lshrrev_b32_e32 v15, 5, v1
	v_bfe_u32 v16, v1, 1, 3
	v_xor_b32_e32 v16, v16, v15
	v_lshlrev_b32_e32 v16, 4, v16
	v_lshl_or_b32 v16, v48, 7, v16
	s_lshl_b32 s18, s13, 13
	s_lshl_b32 s19, s14, 12
	s_add_i32 s19, s19, 0xc000
	v_add_u32_e32 v6, s18, v16
	v_add_u32_e32 v10, s19, v16
	v_xor_b32_e32 v7, 0x20, v6
	v_xor_b32_e32 v11, 0x20, v10
	v_xor_b32_e32 v8, 0x40, v6
	v_xor_b32_e32 v12, 0x40, v10
	v_xor_b32_e32 v9, 0x60, v6
	v_xor_b32_e32 v13, 0x60, v10
	v_lshlrev_b32_e32 v15, 14, v15
	v_lshl_or_b32 v15, v48, 2, v15
	v_accvgpr_write_b32 a0, 0
	v_accvgpr_write_b32 a1, 0
	v_accvgpr_write_b32 a2, 0
	v_accvgpr_write_b32 a3, 0
	v_accvgpr_write_b32 a4, 0
	v_accvgpr_write_b32 a5, 0
	v_accvgpr_write_b32 a6, 0
	v_accvgpr_write_b32 a7, 0
	v_accvgpr_write_b32 a8, 0
	v_accvgpr_write_b32 a9, 0
	v_accvgpr_write_b32 a10, 0
	v_accvgpr_write_b32 a11, 0
	v_accvgpr_write_b32 a12, 0
	v_accvgpr_write_b32 a13, 0
	v_accvgpr_write_b32 a14, 0
	v_accvgpr_write_b32 a15, 0
	v_accvgpr_write_b32 a16, 0
	v_accvgpr_write_b32 a17, 0
	v_accvgpr_write_b32 a18, 0
	v_accvgpr_write_b32 a19, 0
	v_accvgpr_write_b32 a20, 0
	v_accvgpr_write_b32 a21, 0
	v_accvgpr_write_b32 a22, 0
	v_accvgpr_write_b32 a23, 0
	v_accvgpr_write_b32 a24, 0
	v_accvgpr_write_b32 a25, 0
	v_accvgpr_write_b32 a26, 0
	v_accvgpr_write_b32 a27, 0
	v_accvgpr_write_b32 a28, 0
	v_accvgpr_write_b32 a29, 0
	v_accvgpr_write_b32 a30, 0
	v_accvgpr_write_b32 a31, 0
	s_waitcnt vmcnt(6)
	s_barrier
	s_setprio 1
	ds_read_b128 v[16:19], v6 offset:0
	ds_read_b128 v[20:23], v6 offset:4096
	ds_read_b128 v[24:27], v10 offset:0
	s_add_u32 m0, s20, 0x8000
	ds_read_b128 v[28:31], v7 offset:0
	global_load_lds_dwordx4 v2, s[4:5]
	s_add_u32 m0, s20, 0x8400
	ds_read_b128 v[32:35], v7 offset:4096
	global_load_lds_dwordx4 v3, s[4:5]
	s_add_u32 m0, s20, 0x8800
	ds_read_b128 v[36:39], v11 offset:0
	global_load_lds_dwordx4 v4, s[4:5]
	s_add_u32 m0, s20, 0x8c00
	ds_read_b128 v[40:43], v8 offset:0
	global_load_lds_dwordx4 v5, s[4:5]
	s_add_u32 m0, s21, 0x4000
	ds_read_b128 v[44:47], v8 offset:4096
	global_load_lds_dwordx4 v2, s[6:7]
	s_add_u32 m0, s21, 0x4400
	ds_read_b128 v[48:51], v12 offset:0
	global_load_lds_dwordx4 v3, s[6:7]
	ds_read_b128 v[52:55], v9 offset:0
	ds_read_b128 v[56:59], v9 offset:4096
	ds_read_b128 v[60:63], v13 offset:0
	s_add_u32 s4, s4, 0x80
	s_addc_u32 s5, s5, 0
	s_add_u32 s6, s6, 0x80
	s_addc_u32 s7, s7, 0
	s_setprio 0
	s_waitcnt lgkmcnt(9)
	v_mfma_f32_32x32x16_f16 a[0:15], v[16:19], v[24:27], a[0:15]
	v_mfma_f32_32x32x16_f16 a[16:31], v[20:23], v[24:27], a[16:31]
	s_waitcnt lgkmcnt(6)
	v_mfma_f32_32x32x16_f16 a[0:15], v[28:31], v[36:39], a[0:15]
	v_mfma_f32_32x32x16_f16 a[16:31], v[32:35], v[36:39], a[16:31]
	s_waitcnt lgkmcnt(3)
	v_mfma_f32_32x32x16_f16 a[0:15], v[40:43], v[48:51], a[0:15]
	v_mfma_f32_32x32x16_f16 a[16:31], v[44:47], v[48:51], a[16:31]
	s_waitcnt lgkmcnt(0)
	v_mfma_f32_32x32x16_f16 a[0:15], v[52:55], v[60:63], a[0:15]
	v_mfma_f32_32x32x16_f16 a[16:31], v[56:59], v[60:63], a[16:31]
	s_waitcnt vmcnt(6)
	s_barrier
	s_setprio 1
	ds_read_b128 v[16:19], v6 offset:16384
	ds_read_b128 v[20:23], v6 offset:20480
	ds_read_b128 v[24:27], v10 offset:8192
	s_add_u32 m0, s20, 0x0
	ds_read_b128 v[28:31], v7 offset:16384
	global_load_lds_dwordx4 v2, s[4:5]
	s_add_u32 m0, s20, 0x400
	ds_read_b128 v[32:35], v7 offset:20480
	global_load_lds_dwordx4 v3, s[4:5]
	s_add_u32 m0, s20, 0x800
	ds_read_b128 v[36:39], v11 offset:8192
	global_load_lds_dwordx4 v4, s[4:5]
	s_add_u32 m0, s20, 0xc00
	ds_read_b128 v[40:43], v8 offset:16384
	global_load_lds_dwordx4 v5, s[4:5]
	s_add_u32 m0, s21, 0x0
	ds_read_b128 v[44:47], v8 offset:20480
	global_load_lds_dwordx4 v2, s[6:7]
	s_add_u32 m0, s21, 0x400
	ds_read_b128 v[48:51], v12 offset:8192
	global_load_lds_dwordx4 v3, s[6:7]
	ds_read_b128 v[52:55], v9 offset:16384
	ds_read_b128 v[56:59], v9 offset:20480
	ds_read_b128 v[60:63], v13 offset:8192
	s_add_u32 s4, s4, 0x80
	s_addc_u32 s5, s5, 0
	s_add_u32 s6, s6, 0x80
	s_addc_u32 s7, s7, 0
	s_setprio 0
	s_waitcnt lgkmcnt(9)
	v_mfma_f32_32x32x16_f16 a[0:15], v[16:19], v[24:27], a[0:15]
	v_mfma_f32_32x32x16_f16 a[16:31], v[20:23], v[24:27], a[16:31]
	s_waitcnt lgkmcnt(6)
	v_mfma_f32_32x32x16_f16 a[0:15], v[28:31], v[36:39], a[0:15]
	v_mfma_f32_32x32x16_f16 a[16:31], v[32:35], v[36:39], a[16:31]
	s_waitcnt lgkmcnt(3)
	v_mfma_f32_32x32x16_f16 a[0:15], v[40:43], v[48:51], a[0:15]
	v_mfma_f32_32x32x16_f16 a[16:31], v[44:47], v[48:51], a[16:31]
	s_waitcnt lgkmcnt(0)
	v_mfma_f32_32x32x16_f16 a[0:15], v[52:55], v[60:63], a[0:15]
	v_mfma_f32_32x32x16_f16 a[16:31], v[56:59], v[60:63], a[16:31]
	s_waitcnt vmcnt(6)
	s_barrier
	s_setprio 1
	ds_read_b128 v[16:19], v6 offset:32768
	ds_read_b128 v[20:23], v6 offset:36864
	ds_read_b128 v[24:27], v10 offset:16384
	s_add_u32 m0, s20, 0x4000
	ds_read_b128 v[28:31], v7 offset:32768
	global_load_lds_dwordx4 v2, s[4:5]
	s_add_u32 m0, s20, 0x4400
	ds_read_b128 v[32:35], v7 offset:36864
	global_load_lds_dwordx4 v3, s[4:5]
	s_add_u32 m0, s20, 0x4800
	ds_read_b128 v[36:39], v11 offset:16384
	global_load_lds_dwordx4 v4, s[4:5]
	s_add_u32 m0, s20, 0x4c00
	ds_read_b128 v[40:43], v8 offset:32768
	global_load_lds_dwordx4 v5, s[4:5]
	s_add_u32 m0, s21, 0x2000
	ds_read_b128 v[44:47], v8 offset:36864
	global_load_lds_dwordx4 v2, s[6:7]
	s_add_u32 m0, s21, 0x2400
	ds_read_b128 v[48:51], v12 offset:16384
	global_load_lds_dwordx4 v3, s[6:7]
	ds_read_b128 v[52:55], v9 offset:32768
	ds_read_b128 v[56:59], v9 offset:36864
	ds_read_b128 v[60:63], v13 offset:16384
	s_add_u32 s4, s4, 0x80
	s_addc_u32 s5, s5, 0
	s_add_u32 s6, s6, 0x80
	s_addc_u32 s7, s7, 0
	s_setprio 0
	s_waitcnt lgkmcnt(9)
	v_mfma_f32_32x32x16_f16 a[0:15], v[16:19], v[24:27], a[0:15]
	v_mfma_f32_32x32x16_f16 a[16:31], v[20:23], v[24:27], a[16:31]
	s_waitcnt lgkmcnt(6)
	v_mfma_f32_32x32x16_f16 a[0:15], v[28:31], v[36:39], a[0:15]
	v_mfma_f32_32x32x16_f16 a[16:31], v[32:35], v[36:39], a[16:31]
	s_waitcnt lgkmcnt(3)
	v_mfma_f32_32x32x16_f16 a[0:15], v[40:43], v[48:51], a[0:15]
	v_mfma_f32_32x32x16_f16 a[16:31], v[44:47], v[48:51], a[16:31]
	s_waitcnt lgkmcnt(0)
	v_mfma_f32_32x32x16_f16 a[0:15], v[52:55], v[60:63], a[0:15]
	v_mfma_f32_32x32x16_f16 a[16:31], v[56:59], v[60:63], a[16:31]
	s_waitcnt vmcnt(6)
	s_barrier
	s_setprio 1
	ds_read_b128 v[16:19], v6 offset:0
	ds_read_b128 v[20:23], v6 offset:4096
	ds_read_b128 v[24:27], v10 offset:0
	s_add_u32 m0, s20, 0x8000
	ds_read_b128 v[28:31], v7 offset:0
	global_load_lds_dwordx4 v2, s[4:5]
	s_add_u32 m0, s20, 0x8400
	ds_read_b128 v[32:35], v7 offset:4096
	global_load_lds_dwordx4 v3, s[4:5]
	s_add_u32 m0, s20, 0x8800
	ds_read_b128 v[36:39], v11 offset:0
	global_load_lds_dwordx4 v4, s[4:5]
	s_add_u32 m0, s20, 0x8c00
	ds_read_b128 v[40:43], v8 offset:0
	global_load_lds_dwordx4 v5, s[4:5]
	s_add_u32 m0, s21, 0x4000
	ds_read_b128 v[44:47], v8 offset:4096
	global_load_lds_dwordx4 v2, s[6:7]
	s_add_u32 m0, s21, 0x4400
	ds_read_b128 v[48:51], v12 offset:0
	global_load_lds_dwordx4 v3, s[6:7]
	ds_read_b128 v[52:55], v9 offset:0
	ds_read_b128 v[56:59], v9 offset:4096
	ds_read_b128 v[60:63], v13 offset:0
	s_add_u32 s4, s4, 0x80
	s_addc_u32 s5, s5, 0
	s_add_u32 s6, s6, 0x80
	s_addc_u32 s7, s7, 0
	s_setprio 0
	s_waitcnt lgkmcnt(9)
	v_mfma_f32_32x32x16_f16 a[0:15], v[16:19], v[24:27], a[0:15]
	v_mfma_f32_32x32x16_f16 a[16:31], v[20:23], v[24:27], a[16:31]
	s_waitcnt lgkmcnt(6)
	v_mfma_f32_32x32x16_f16 a[0:15], v[28:31], v[36:39], a[0:15]
	v_mfma_f32_32x32x16_f16 a[16:31], v[32:35], v[36:39], a[16:31]
	s_waitcnt lgkmcnt(3)
	v_mfma_f32_32x32x16_f16 a[0:15], v[40:43], v[48:51], a[0:15]
	v_mfma_f32_32x32x16_f16 a[16:31], v[44:47], v[48:51], a[16:31]
	s_waitcnt lgkmcnt(0)
	v_mfma_f32_32x32x16_f16 a[0:15], v[52:55], v[60:63], a[0:15]
	v_mfma_f32_32x32x16_f16 a[16:31], v[56:59], v[60:63], a[16:31]
	s_waitcnt vmcnt(6)
	s_barrier
	s_setprio 1
	ds_read_b128 v[16:19], v6 offset:16384
	ds_read_b128 v[20:23], v6 offset:20480
	ds_read_b128 v[24:27], v10 offset:8192
	s_add_u32 m0, s20, 0x0
	ds_read_b128 v[28:31], v7 offset:16384
	global_load_lds_dwordx4 v2, s[4:5]
	s_add_u32 m0, s20, 0x400
	ds_read_b128 v[32:35], v7 offset:20480
	global_load_lds_dwordx4 v3, s[4:5]
	s_add_u32 m0, s20, 0x800
	ds_read_b128 v[36:39], v11 offset:8192
	global_load_lds_dwordx4 v4, s[4:5]
	s_add_u32 m0, s20, 0xc00
	ds_read_b128 v[40:43], v8 offset:16384
	global_load_lds_dwordx4 v5, s[4:5]
	s_add_u32 m0, s21, 0x0
	ds_read_b128 v[44:47], v8 offset:20480
	global_load_lds_dwordx4 v2, s[6:7]
	s_add_u32 m0, s21, 0x400
	ds_read_b128 v[48:51], v12 offset:8192
	global_load_lds_dwordx4 v3, s[6:7]
	ds_read_b128 v[52:55], v9 offset:16384
	ds_read_b128 v[56:59], v9 offset:20480
	ds_read_b128 v[60:63], v13 offset:8192
	s_add_u32 s4, s4, 0x80
	s_addc_u32 s5, s5, 0
	s_add_u32 s6, s6, 0x80
	s_addc_u32 s7, s7, 0
	s_setprio 0
	s_waitcnt lgkmcnt(9)
	v_mfma_f32_32x32x16_f16 a[0:15], v[16:19], v[24:27], a[0:15]
	v_mfma_f32_32x32x16_f16 a[16:31], v[20:23], v[24:27], a[16:31]
	s_waitcnt lgkmcnt(6)
	v_mfma_f32_32x32x16_f16 a[0:15], v[28:31], v[36:39], a[0:15]
	v_mfma_f32_32x32x16_f16 a[16:31], v[32:35], v[36:39], a[16:31]
	s_waitcnt lgkmcnt(3)
	v_mfma_f32_32x32x16_f16 a[0:15], v[40:43], v[48:51], a[0:15]
	v_mfma_f32_32x32x16_f16 a[16:31], v[44:47], v[48:51], a[16:31]
	s_waitcnt lgkmcnt(0)
	v_mfma_f32_32x32x16_f16 a[0:15], v[52:55], v[60:63], a[0:15]
	v_mfma_f32_32x32x16_f16 a[16:31], v[56:59], v[60:63], a[16:31]
	s_waitcnt vmcnt(6)
	s_barrier
	s_setprio 1
	ds_read_b128 v[16:19], v6 offset:32768
	ds_read_b128 v[20:23], v6 offset:36864
	ds_read_b128 v[24:27], v10 offset:16384
	s_add_u32 m0, s20, 0x4000
	ds_read_b128 v[28:31], v7 offset:32768
	global_load_lds_dwordx4 v2, s[4:5]
	s_add_u32 m0, s20, 0x4400
	ds_read_b128 v[32:35], v7 offset:36864
	global_load_lds_dwordx4 v3, s[4:5]
	s_add_u32 m0, s20, 0x4800
	ds_read_b128 v[36:39], v11 offset:16384
	global_load_lds_dwordx4 v4, s[4:5]
	s_add_u32 m0, s20, 0x4c00
	ds_read_b128 v[40:43], v8 offset:32768
	global_load_lds_dwordx4 v5, s[4:5]
	s_add_u32 m0, s21, 0x2000
	ds_read_b128 v[44:47], v8 offset:36864
	global_load_lds_dwordx4 v2, s[6:7]
	s_add_u32 m0, s21, 0x2400
	ds_read_b128 v[48:51], v12 offset:16384
	global_load_lds_dwordx4 v3, s[6:7]
	ds_read_b128 v[52:55], v9 offset:32768
	ds_read_b128 v[56:59], v9 offset:36864
	ds_read_b128 v[60:63], v13 offset:16384
	s_add_u32 s4, s4, 0x80
	s_addc_u32 s5, s5, 0
	s_add_u32 s6, s6, 0x80
	s_addc_u32 s7, s7, 0
	s_setprio 0
	s_waitcnt lgkmcnt(9)
	v_mfma_f32_32x32x16_f16 a[0:15], v[16:19], v[24:27], a[0:15]
	v_mfma_f32_32x32x16_f16 a[16:31], v[20:23], v[24:27], a[16:31]
	s_waitcnt lgkmcnt(6)
	v_mfma_f32_32x32x16_f16 a[0:15], v[28:31], v[36:39], a[0:15]
	v_mfma_f32_32x32x16_f16 a[16:31], v[32:35], v[36:39], a[16:31]
	s_waitcnt lgkmcnt(3)
	v_mfma_f32_32x32x16_f16 a[0:15], v[40:43], v[48:51], a[0:15]
	v_mfma_f32_32x32x16_f16 a[16:31], v[44:47], v[48:51], a[16:31]
	s_waitcnt lgkmcnt(0)
	v_mfma_f32_32x32x16_f16 a[0:15], v[52:55], v[60:63], a[0:15]
	v_mfma_f32_32x32x16_f16 a[16:31], v[56:59], v[60:63], a[16:31]
	s_waitcnt vmcnt(6)
	s_barrier
	s_setprio 1
	ds_read_b128 v[16:19], v6 offset:0
	ds_read_b128 v[20:23], v6 offset:4096
	ds_read_b128 v[24:27], v10 offset:0
	s_add_u32 m0, s20, 0x8000
	ds_read_b128 v[28:31], v7 offset:0
	global_load_lds_dwordx4 v2, s[4:5]
	s_add_u32 m0, s20, 0x8400
	ds_read_b128 v[32:35], v7 offset:4096
	global_load_lds_dwordx4 v3, s[4:5]
	s_add_u32 m0, s20, 0x8800
	ds_read_b128 v[36:39], v11 offset:0
	global_load_lds_dwordx4 v4, s[4:5]
	s_add_u32 m0, s20, 0x8c00
	ds_read_b128 v[40:43], v8 offset:0
	global_load_lds_dwordx4 v5, s[4:5]
	s_add_u32 m0, s21, 0x4000
	ds_read_b128 v[44:47], v8 offset:4096
	global_load_lds_dwordx4 v2, s[6:7]
	s_add_u32 m0, s21, 0x4400
	ds_read_b128 v[48:51], v12 offset:0
	global_load_lds_dwordx4 v3, s[6:7]
	ds_read_b128 v[52:55], v9 offset:0
	ds_read_b128 v[56:59], v9 offset:4096
	ds_read_b128 v[60:63], v13 offset:0
	s_add_u32 s4, s4, 0x80
	s_addc_u32 s5, s5, 0
	s_add_u32 s6, s6, 0x80
	s_addc_u32 s7, s7, 0
	s_setprio 0
	s_waitcnt lgkmcnt(9)
	v_mfma_f32_32x32x16_f16 a[0:15], v[16:19], v[24:27], a[0:15]
	v_mfma_f32_32x32x16_f16 a[16:31], v[20:23], v[24:27], a[16:31]
	s_waitcnt lgkmcnt(6)
	v_mfma_f32_32x32x16_f16 a[0:15], v[28:31], v[36:39], a[0:15]
	v_mfma_f32_32x32x16_f16 a[16:31], v[32:35], v[36:39], a[16:31]
	s_waitcnt lgkmcnt(3)
	v_mfma_f32_32x32x16_f16 a[0:15], v[40:43], v[48:51], a[0:15]
	v_mfma_f32_32x32x16_f16 a[16:31], v[44:47], v[48:51], a[16:31]
	s_waitcnt lgkmcnt(0)
	v_mfma_f32_32x32x16_f16 a[0:15], v[52:55], v[60:63], a[0:15]
	v_mfma_f32_32x32x16_f16 a[16:31], v[56:59], v[60:63], a[16:31]
	s_waitcnt vmcnt(6)
	s_barrier
	s_setprio 1
	ds_read_b128 v[16:19], v6 offset:16384
	ds_read_b128 v[20:23], v6 offset:20480
	ds_read_b128 v[24:27], v10 offset:8192
	s_add_u32 m0, s20, 0x0
	ds_read_b128 v[28:31], v7 offset:16384
	global_load_lds_dwordx4 v2, s[4:5]
	s_add_u32 m0, s20, 0x400
	ds_read_b128 v[32:35], v7 offset:20480
	global_load_lds_dwordx4 v3, s[4:5]
	s_add_u32 m0, s20, 0x800
	ds_read_b128 v[36:39], v11 offset:8192
	global_load_lds_dwordx4 v4, s[4:5]
	s_add_u32 m0, s20, 0xc00
	ds_read_b128 v[40:43], v8 offset:16384
	global_load_lds_dwordx4 v5, s[4:5]
	s_add_u32 m0, s21, 0x0
	ds_read_b128 v[44:47], v8 offset:20480
	global_load_lds_dwordx4 v2, s[6:7]
	s_add_u32 m0, s21, 0x400
	ds_read_b128 v[48:51], v12 offset:8192
	global_load_lds_dwordx4 v3, s[6:7]
	ds_read_b128 v[52:55], v9 offset:16384
	ds_read_b128 v[56:59], v9 offset:20480
	ds_read_b128 v[60:63], v13 offset:8192
	s_add_u32 s4, s4, 0x80
	s_addc_u32 s5, s5, 0
	s_add_u32 s6, s6, 0x80
	s_addc_u32 s7, s7, 0
	s_setprio 0
	s_waitcnt lgkmcnt(9)
	v_mfma_f32_32x32x16_f16 a[0:15], v[16:19], v[24:27], a[0:15]
	v_mfma_f32_32x32x16_f16 a[16:31], v[20:23], v[24:27], a[16:31]
	s_waitcnt lgkmcnt(6)
	v_mfma_f32_32x32x16_f16 a[0:15], v[28:31], v[36:39], a[0:15]
	v_mfma_f32_32x32x16_f16 a[16:31], v[32:35], v[36:39], a[16:31]
	s_waitcnt lgkmcnt(3)
	v_mfma_f32_32x32x16_f16 a[0:15], v[40:43], v[48:51], a[0:15]
	v_mfma_f32_32x32x16_f16 a[16:31], v[44:47], v[48:51], a[16:31]
	s_waitcnt lgkmcnt(0)
	v_mfma_f32_32x32x16_f16 a[0:15], v[52:55], v[60:63], a[0:15]
	v_mfma_f32_32x32x16_f16 a[16:31], v[56:59], v[60:63], a[16:31]
	s_waitcnt vmcnt(6)
	s_barrier
	s_setprio 1
	ds_read_b128 v[16:19], v6 offset:32768
	ds_read_b128 v[20:23], v6 offset:36864
	ds_read_b128 v[24:27], v10 offset:16384
	s_add_u32 m0, s20, 0x4000
	ds_read_b128 v[28:31], v7 offset:32768
	global_load_lds_dwordx4 v2, s[4:5]
	s_add_u32 m0, s20, 0x4400
	ds_read_b128 v[32:35], v7 offset:36864
	global_load_lds_dwordx4 v3, s[4:5]
	s_add_u32 m0, s20, 0x4800
	ds_read_b128 v[36:39], v11 offset:16384
	global_load_lds_dwordx4 v4, s[4:5]
	s_add_u32 m0, s20, 0x4c00
	ds_read_b128 v[40:43], v8 offset:32768
	global_load_lds_dwordx4 v5, s[4:5]
	s_add_u32 m0, s21, 0x2000
	ds_read_b128 v[44:47], v8 offset:36864
	global_load_lds_dwordx4 v2, s[6:7]
	s_add_u32 m0, s21, 0x2400
	ds_read_b128 v[48:51], v12 offset:16384
	global_load_lds_dwordx4 v3, s[6:7]
	ds_read_b128 v[52:55], v9 offset:32768
	ds_read_b128 v[56:59], v9 offset:36864
	ds_read_b128 v[60:63], v13 offset:16384
	s_add_u32 s4, s4, 0x80
	s_addc_u32 s5, s5, 0
	s_add_u32 s6, s6, 0x80
	s_addc_u32 s7, s7, 0
	s_setprio 0
	s_waitcnt lgkmcnt(9)
	v_mfma_f32_32x32x16_f16 a[0:15], v[16:19], v[24:27], a[0:15]
	v_mfma_f32_32x32x16_f16 a[16:31], v[20:23], v[24:27], a[16:31]
	s_waitcnt lgkmcnt(6)
	v_mfma_f32_32x32x16_f16 a[0:15], v[28:31], v[36:39], a[0:15]
	v_mfma_f32_32x32x16_f16 a[16:31], v[32:35], v[36:39], a[16:31]
	s_waitcnt lgkmcnt(3)
	v_mfma_f32_32x32x16_f16 a[0:15], v[40:43], v[48:51], a[0:15]
	v_mfma_f32_32x32x16_f16 a[16:31], v[44:47], v[48:51], a[16:31]
	s_waitcnt lgkmcnt(0)
	v_mfma_f32_32x32x16_f16 a[0:15], v[52:55], v[60:63], a[0:15]
	v_mfma_f32_32x32x16_f16 a[16:31], v[56:59], v[60:63], a[16:31]
	s_waitcnt vmcnt(6)
	s_barrier
	s_setprio 1
	ds_read_b128 v[16:19], v6 offset:0
	ds_read_b128 v[20:23], v6 offset:4096
	ds_read_b128 v[24:27], v10 offset:0
	s_add_u32 m0, s20, 0x8000
	ds_read_b128 v[28:31], v7 offset:0
	global_load_lds_dwordx4 v2, s[4:5]
	s_add_u32 m0, s20, 0x8400
	ds_read_b128 v[32:35], v7 offset:4096
	global_load_lds_dwordx4 v3, s[4:5]
	s_add_u32 m0, s20, 0x8800
	ds_read_b128 v[36:39], v11 offset:0
	global_load_lds_dwordx4 v4, s[4:5]
	s_add_u32 m0, s20, 0x8c00
	ds_read_b128 v[40:43], v8 offset:0
	global_load_lds_dwordx4 v5, s[4:5]
	s_add_u32 m0, s21, 0x4000
	ds_read_b128 v[44:47], v8 offset:4096
	global_load_lds_dwordx4 v2, s[6:7]
	s_add_u32 m0, s21, 0x4400
	ds_read_b128 v[48:51], v12 offset:0
	global_load_lds_dwordx4 v3, s[6:7]
	ds_read_b128 v[52:55], v9 offset:0
	ds_read_b128 v[56:59], v9 offset:4096
	ds_read_b128 v[60:63], v13 offset:0
	s_add_u32 s4, s4, 0x80
	s_addc_u32 s5, s5, 0
	s_add_u32 s6, s6, 0x80
	s_addc_u32 s7, s7, 0
	s_setprio 0
	s_waitcnt lgkmcnt(9)
	v_mfma_f32_32x32x16_f16 a[0:15], v[16:19], v[24:27], a[0:15]
	v_mfma_f32_32x32x16_f16 a[16:31], v[20:23], v[24:27], a[16:31]
	s_waitcnt lgkmcnt(6)
	v_mfma_f32_32x32x16_f16 a[0:15], v[28:31], v[36:39], a[0:15]
	v_mfma_f32_32x32x16_f16 a[16:31], v[32:35], v[36:39], a[16:31]
	s_waitcnt lgkmcnt(3)
	v_mfma_f32_32x32x16_f16 a[0:15], v[40:43], v[48:51], a[0:15]
	v_mfma_f32_32x32x16_f16 a[16:31], v[44:47], v[48:51], a[16:31]
	s_waitcnt lgkmcnt(0)
	v_mfma_f32_32x32x16_f16 a[0:15], v[52:55], v[60:63], a[0:15]
	v_mfma_f32_32x32x16_f16 a[16:31], v[56:59], v[60:63], a[16:31]
	s_waitcnt vmcnt(6)
	s_barrier
	s_setprio 1
	ds_read_b128 v[16:19], v6 offset:16384
	ds_read_b128 v[20:23], v6 offset:20480
	ds_read_b128 v[24:27], v10 offset:8192
	s_add_u32 m0, s20, 0x0
	ds_read_b128 v[28:31], v7 offset:16384
	global_load_lds_dwordx4 v2, s[4:5]
	s_add_u32 m0, s20, 0x400
	ds_read_b128 v[32:35], v7 offset:20480
	global_load_lds_dwordx4 v3, s[4:5]
	s_add_u32 m0, s20, 0x800
	ds_read_b128 v[36:39], v11 offset:8192
	global_load_lds_dwordx4 v4, s[4:5]
	s_add_u32 m0, s20, 0xc00
	ds_read_b128 v[40:43], v8 offset:16384
	global_load_lds_dwordx4 v5, s[4:5]
	s_add_u32 m0, s21, 0x0
	ds_read_b128 v[44:47], v8 offset:20480
	global_load_lds_dwordx4 v2, s[6:7]
	s_add_u32 m0, s21, 0x400
	ds_read_b128 v[48:51], v12 offset:8192
	global_load_lds_dwordx4 v3, s[6:7]
	ds_read_b128 v[52:55], v9 offset:16384
	ds_read_b128 v[56:59], v9 offset:20480
	ds_read_b128 v[60:63], v13 offset:8192
	s_add_u32 s4, s4, 0x80
	s_addc_u32 s5, s5, 0
	s_add_u32 s6, s6, 0x80
	s_addc_u32 s7, s7, 0
	s_setprio 0
	s_waitcnt lgkmcnt(9)
	v_mfma_f32_32x32x16_f16 a[0:15], v[16:19], v[24:27], a[0:15]
	v_mfma_f32_32x32x16_f16 a[16:31], v[20:23], v[24:27], a[16:31]
	s_waitcnt lgkmcnt(6)
	v_mfma_f32_32x32x16_f16 a[0:15], v[28:31], v[36:39], a[0:15]
	v_mfma_f32_32x32x16_f16 a[16:31], v[32:35], v[36:39], a[16:31]
	s_waitcnt lgkmcnt(3)
	v_mfma_f32_32x32x16_f16 a[0:15], v[40:43], v[48:51], a[0:15]
	v_mfma_f32_32x32x16_f16 a[16:31], v[44:47], v[48:51], a[16:31]
	s_waitcnt lgkmcnt(0)
	v_mfma_f32_32x32x16_f16 a[0:15], v[52:55], v[60:63], a[0:15]
	v_mfma_f32_32x32x16_f16 a[16:31], v[56:59], v[60:63], a[16:31]
	s_waitcnt vmcnt(6)
	s_barrier
	s_setprio 1
	ds_read_b128 v[16:19], v6 offset:32768
	ds_read_b128 v[20:23], v6 offset:36864
	ds_read_b128 v[24:27], v10 offset:16384
	s_add_u32 m0, s20, 0x4000
	ds_read_b128 v[28:31], v7 offset:32768
	global_load_lds_dwordx4 v2, s[4:5]
	s_add_u32 m0, s20, 0x4400
	ds_read_b128 v[32:35], v7 offset:36864
	global_load_lds_dwordx4 v3, s[4:5]
	s_add_u32 m0, s20, 0x4800
	ds_read_b128 v[36:39], v11 offset:16384
	global_load_lds_dwordx4 v4, s[4:5]
	s_add_u32 m0, s20, 0x4c00
	ds_read_b128 v[40:43], v8 offset:32768
	global_load_lds_dwordx4 v5, s[4:5]
	s_add_u32 m0, s21, 0x2000
	ds_read_b128 v[44:47], v8 offset:36864
	global_load_lds_dwordx4 v2, s[6:7]
	s_add_u32 m0, s21, 0x2400
	ds_read_b128 v[48:51], v12 offset:16384
	global_load_lds_dwordx4 v3, s[6:7]
	ds_read_b128 v[52:55], v9 offset:32768
	ds_read_b128 v[56:59], v9 offset:36864
	ds_read_b128 v[60:63], v13 offset:16384
	s_add_u32 s4, s4, 0x80
	s_addc_u32 s5, s5, 0
	s_add_u32 s6, s6, 0x80
	s_addc_u32 s7, s7, 0
	s_setprio 0
	s_waitcnt lgkmcnt(9)
	v_mfma_f32_32x32x16_f16 a[0:15], v[16:19], v[24:27], a[0:15]
	v_mfma_f32_32x32x16_f16 a[16:31], v[20:23], v[24:27], a[16:31]
	s_waitcnt lgkmcnt(6)
	v_mfma_f32_32x32x16_f16 a[0:15], v[28:31], v[36:39], a[0:15]
	v_mfma_f32_32x32x16_f16 a[16:31], v[32:35], v[36:39], a[16:31]
	s_waitcnt lgkmcnt(3)
	v_mfma_f32_32x32x16_f16 a[0:15], v[40:43], v[48:51], a[0:15]
	v_mfma_f32_32x32x16_f16 a[16:31], v[44:47], v[48:51], a[16:31]
	s_waitcnt lgkmcnt(0)
	v_mfma_f32_32x32x16_f16 a[0:15], v[52:55], v[60:63], a[0:15]
	v_mfma_f32_32x32x16_f16 a[16:31], v[56:59], v[60:63], a[16:31]
	s_waitcnt vmcnt(6)
	s_barrier
	s_setprio 1
	ds_read_b128 v[16:19], v6 offset:0
	ds_read_b128 v[20:23], v6 offset:4096
	ds_read_b128 v[24:27], v10 offset:0
	s_add_u32 m0, s20, 0x8000
	ds_read_b128 v[28:31], v7 offset:0
	global_load_lds_dwordx4 v2, s[4:5]
	s_add_u32 m0, s20, 0x8400
	ds_read_b128 v[32:35], v7 offset:4096
	global_load_lds_dwordx4 v3, s[4:5]
	s_add_u32 m0, s20, 0x8800
	ds_read_b128 v[36:39], v11 offset:0
	global_load_lds_dwordx4 v4, s[4:5]
	s_add_u32 m0, s20, 0x8c00
	ds_read_b128 v[40:43], v8 offset:0
	global_load_lds_dwordx4 v5, s[4:5]
	s_add_u32 m0, s21, 0x4000
	ds_read_b128 v[44:47], v8 offset:4096
	global_load_lds_dwordx4 v2, s[6:7]
	s_add_u32 m0, s21, 0x4400
	ds_read_b128 v[48:51], v12 offset:0
	global_load_lds_dwordx4 v3, s[6:7]
	ds_read_b128 v[52:55], v9 offset:0
	ds_read_b128 v[56:59], v9 offset:4096
	ds_read_b128 v[60:63], v13 offset:0
	s_add_u32 s4, s4, 0x80
	s_addc_u32 s5, s5, 0
	s_add_u32 s6, s6, 0x80
	s_addc_u32 s7, s7, 0
	s_setprio 0
	s_waitcnt lgkmcnt(9)
	v_mfma_f32_32x32x16_f16 a[0:15], v[16:19], v[24:27], a[0:15]
	v_mfma_f32_32x32x16_f16 a[16:31], v[20:23], v[24:27], a[16:31]
	s_waitcnt lgkmcnt(6)
	v_mfma_f32_32x32x16_f16 a[0:15], v[28:31], v[36:39], a[0:15]
	v_mfma_f32_32x32x16_f16 a[16:31], v[32:35], v[36:39], a[16:31]
	s_waitcnt lgkmcnt(3)
	v_mfma_f32_32x32x16_f16 a[0:15], v[40:43], v[48:51], a[0:15]
	v_mfma_f32_32x32x16_f16 a[16:31], v[44:47], v[48:51], a[16:31]
	s_waitcnt lgkmcnt(0)
	v_mfma_f32_32x32x16_f16 a[0:15], v[52:55], v[60:63], a[0:15]
	v_mfma_f32_32x32x16_f16 a[16:31], v[56:59], v[60:63], a[16:31]
	s_waitcnt vmcnt(6)
	s_barrier
	s_setprio 1
	ds_read_b128 v[16:19], v6 offset:16384
	ds_read_b128 v[20:23], v6 offset:20480
	ds_read_b128 v[24:27], v10 offset:8192
	s_add_u32 m0, s20, 0x0
	ds_read_b128 v[28:31], v7 offset:16384
	global_load_lds_dwordx4 v2, s[4:5]
	s_add_u32 m0, s20, 0x400
	ds_read_b128 v[32:35], v7 offset:20480
	global_load_lds_dwordx4 v3, s[4:5]
	s_add_u32 m0, s20, 0x800
	ds_read_b128 v[36:39], v11 offset:8192
	global_load_lds_dwordx4 v4, s[4:5]
	s_add_u32 m0, s20, 0xc00
	ds_read_b128 v[40:43], v8 offset:16384
	global_load_lds_dwordx4 v5, s[4:5]
	s_add_u32 m0, s21, 0x0
	ds_read_b128 v[44:47], v8 offset:20480
	global_load_lds_dwordx4 v2, s[6:7]
	s_add_u32 m0, s21, 0x400
	ds_read_b128 v[48:51], v12 offset:8192
	global_load_lds_dwordx4 v3, s[6:7]
	ds_read_b128 v[52:55], v9 offset:16384
	ds_read_b128 v[56:59], v9 offset:20480
	ds_read_b128 v[60:63], v13 offset:8192
	s_add_u32 s4, s4, 0x80
	s_addc_u32 s5, s5, 0
	s_add_u32 s6, s6, 0x80
	s_addc_u32 s7, s7, 0
	s_setprio 0
	s_waitcnt lgkmcnt(9)
	v_mfma_f32_32x32x16_f16 a[0:15], v[16:19], v[24:27], a[0:15]
	v_mfma_f32_32x32x16_f16 a[16:31], v[20:23], v[24:27], a[16:31]
	s_waitcnt lgkmcnt(6)
	v_mfma_f32_32x32x16_f16 a[0:15], v[28:31], v[36:39], a[0:15]
	v_mfma_f32_32x32x16_f16 a[16:31], v[32:35], v[36:39], a[16:31]
	s_waitcnt lgkmcnt(3)
	v_mfma_f32_32x32x16_f16 a[0:15], v[40:43], v[48:51], a[0:15]
	v_mfma_f32_32x32x16_f16 a[16:31], v[44:47], v[48:51], a[16:31]
	s_waitcnt lgkmcnt(0)
	v_mfma_f32_32x32x16_f16 a[0:15], v[52:55], v[60:63], a[0:15]
	v_mfma_f32_32x32x16_f16 a[16:31], v[56:59], v[60:63], a[16:31]
	s_waitcnt vmcnt(6)
	s_barrier
	s_setprio 1
	ds_read_b128 v[16:19], v6 offset:32768
	ds_read_b128 v[20:23], v6 offset:36864
	ds_read_b128 v[24:27], v10 offset:16384
	ds_read_b128 v[28:31], v7 offset:32768
	ds_read_b128 v[32:35], v7 offset:36864
	ds_read_b128 v[36:39], v11 offset:16384
	ds_read_b128 v[40:43], v8 offset:32768
	ds_read_b128 v[44:47], v8 offset:36864
	ds_read_b128 v[48:51], v12 offset:16384
	ds_read_b128 v[52:55], v9 offset:32768
	ds_read_b128 v[56:59], v9 offset:36864
	ds_read_b128 v[60:63], v13 offset:16384
	s_setprio 0
	s_waitcnt lgkmcnt(9)
	v_mfma_f32_32x32x16_f16 a[0:15], v[16:19], v[24:27], a[0:15]
	v_mfma_f32_32x32x16_f16 a[16:31], v[20:23], v[24:27], a[16:31]
	s_waitcnt lgkmcnt(6)
	v_mfma_f32_32x32x16_f16 a[0:15], v[28:31], v[36:39], a[0:15]
	v_mfma_f32_32x32x16_f16 a[16:31], v[32:35], v[36:39], a[16:31]
	s_waitcnt lgkmcnt(3)
	v_mfma_f32_32x32x16_f16 a[0:15], v[40:43], v[48:51], a[0:15]
	v_mfma_f32_32x32x16_f16 a[16:31], v[44:47], v[48:51], a[16:31]
	s_waitcnt lgkmcnt(0)
	v_mfma_f32_32x32x16_f16 a[0:15], v[52:55], v[60:63], a[0:15]
	v_mfma_f32_32x32x16_f16 a[16:31], v[56:59], v[60:63], a[16:31]
	s_waitcnt vmcnt(0)
	s_barrier
	s_setprio 1
	ds_read_b128 v[16:19], v6 offset:0
	ds_read_b128 v[20:23], v6 offset:4096
	ds_read_b128 v[24:27], v10 offset:0
	ds_read_b128 v[28:31], v7 offset:0
	ds_read_b128 v[32:35], v7 offset:4096
	ds_read_b128 v[36:39], v11 offset:0
	ds_read_b128 v[40:43], v8 offset:0
	ds_read_b128 v[44:47], v8 offset:4096
	ds_read_b128 v[48:51], v12 offset:0
	ds_read_b128 v[52:55], v9 offset:0
	ds_read_b128 v[56:59], v9 offset:4096
	ds_read_b128 v[60:63], v13 offset:0
	s_setprio 0
	s_waitcnt lgkmcnt(9)
	v_mfma_f32_32x32x16_f16 a[0:15], v[16:19], v[24:27], a[0:15]
	v_mfma_f32_32x32x16_f16 a[16:31], v[20:23], v[24:27], a[16:31]
	s_waitcnt lgkmcnt(6)
	v_mfma_f32_32x32x16_f16 a[0:15], v[28:31], v[36:39], a[0:15]
	v_mfma_f32_32x32x16_f16 a[16:31], v[32:35], v[36:39], a[16:31]
	s_waitcnt lgkmcnt(3)
	v_mfma_f32_32x32x16_f16 a[0:15], v[40:43], v[48:51], a[0:15]
	v_mfma_f32_32x32x16_f16 a[16:31], v[44:47], v[48:51], a[16:31]
	s_waitcnt lgkmcnt(0)
	v_mfma_f32_32x32x16_f16 a[0:15], v[52:55], v[60:63], a[0:15]
	v_mfma_f32_32x32x16_f16 a[16:31], v[56:59], v[60:63], a[16:31]
	s_nop 15
	s_nop 3
	v_accvgpr_read_b32 v16, a0
	v_accvgpr_read_b32 v17, a1
	v_accvgpr_read_b32 v18, a2
	v_accvgpr_read_b32 v19, a3
	v_accvgpr_read_b32 v20, a4
	v_accvgpr_read_b32 v21, a5
	v_accvgpr_read_b32 v22, a6
	v_accvgpr_read_b32 v23, a7
	v_accvgpr_read_b32 v24, a8
	v_accvgpr_read_b32 v25, a9
	v_accvgpr_read_b32 v26, a10
	v_accvgpr_read_b32 v27, a11
	v_accvgpr_read_b32 v28, a12
	v_accvgpr_read_b32 v29, a13
	v_accvgpr_read_b32 v30, a14
	v_accvgpr_read_b32 v31, a15
	v_accvgpr_read_b32 v32, a16
	v_accvgpr_read_b32 v33, a17
	v_accvgpr_read_b32 v34, a18
	v_accvgpr_read_b32 v35, a19
	v_accvgpr_read_b32 v36, a20
	v_accvgpr_read_b32 v37, a21
	v_accvgpr_read_b32 v38, a22
	v_accvgpr_read_b32 v39, a23
	v_accvgpr_read_b32 v40, a24
	v_accvgpr_read_b32 v41, a25
	v_accvgpr_read_b32 v42, a26
	v_accvgpr_read_b32 v43, a27
	v_accvgpr_read_b32 v44, a28
	v_accvgpr_read_b32 v45, a29
	v_accvgpr_read_b32 v46, a30
	v_accvgpr_read_b32 v47, a31
	v_add_f32_e32 v16, v14, v16
	v_add_f32_e32 v17, v14, v17
	v_add_f32_e32 v18, v14, v18
	v_add_f32_e32 v19, v14, v19
	v_add_f32_e32 v20, v14, v20
	v_add_f32_e32 v21, v14, v21
	v_add_f32_e32 v22, v14, v22
	v_add_f32_e32 v23, v14, v23
	v_add_f32_e32 v24, v14, v24
	v_add_f32_e32 v25, v14, v25
	v_add_f32_e32 v26, v14, v26
	v_add_f32_e32 v27, v14, v27
	v_add_f32_e32 v28, v14, v28
	v_add_f32_e32 v29, v14, v29
	v_add_f32_e32 v30, v14, v30
	v_add_f32_e32 v31, v14, v31
	v_add_f32_e32 v32, v14, v32
	v_add_f32_e32 v33, v14, v33
	v_add_f32_e32 v34, v14, v34
	v_add_f32_e32 v35, v14, v35
	v_add_f32_e32 v36, v14, v36
	v_add_f32_e32 v37, v14, v37
	v_add_f32_e32 v38, v14, v38
	v_add_f32_e32 v39, v14, v39
	v_add_f32_e32 v40, v14, v40
	v_add_f32_e32 v41, v14, v41
	v_add_f32_e32 v42, v14, v42
	v_add_f32_e32 v43, v14, v43
	v_add_f32_e32 v44, v14, v44
	v_add_f32_e32 v45, v14, v45
	v_add_f32_e32 v46, v14, v46
	v_add_f32_e32 v47, v14, v47
	global_store_dword v15, v16, s[8:9] nt
	s_add_u32 s8, s8, 0x1000
	s_addc_u32 s9, s9, 0
	global_store_dword v15, v17, s[8:9] nt
	s_add_u32 s8, s8, 0x1000
	s_addc_u32 s9, s9, 0
	global_store_dword v15, v18, s[8:9] nt
	s_add_u32 s8, s8, 0x1000
	s_addc_u32 s9, s9, 0
	global_store_dword v15, v19, s[8:9] nt
	s_add_u32 s8, s8, 0x5000
	s_addc_u32 s9, s9, 0
	global_store_dword v15, v20, s[8:9] nt
	s_add_u32 s8, s8, 0x1000
	s_addc_u32 s9, s9, 0
	global_store_dword v15, v21, s[8:9] nt
	s_add_u32 s8, s8, 0x1000
	s_addc_u32 s9, s9, 0
	global_store_dword v15, v22, s[8:9] nt
	s_add_u32 s8, s8, 0x1000
	s_addc_u32 s9, s9, 0
	global_store_dword v15, v23, s[8:9] nt
	s_add_u32 s8, s8, 0x5000
	s_addc_u32 s9, s9, 0
	global_store_dword v15, v24, s[8:9] nt
	s_add_u32 s8, s8, 0x1000
	s_addc_u32 s9, s9, 0
	global_store_dword v15, v25, s[8:9] nt
	s_add_u32 s8, s8, 0x1000
	s_addc_u32 s9, s9, 0
	global_store_dword v15, v26, s[8:9] nt
	s_add_u32 s8, s8, 0x1000
	s_addc_u32 s9, s9, 0
	global_store_dword v15, v27, s[8:9] nt
	s_add_u32 s8, s8, 0x5000
	s_addc_u32 s9, s9, 0
	global_store_dword v15, v28, s[8:9] nt
	s_add_u32 s8, s8, 0x1000
	s_addc_u32 s9, s9, 0
	global_store_dword v15, v29, s[8:9] nt
	s_add_u32 s8, s8, 0x1000
	s_addc_u32 s9, s9, 0
	global_store_dword v15, v30, s[8:9] nt
	s_add_u32 s8, s8, 0x1000
	s_addc_u32 s9, s9, 0
	global_store_dword v15, v31, s[8:9] nt
	s_add_u32 s8, s8, 0x5000
	s_addc_u32 s9, s9, 0
	global_store_dword v15, v32, s[8:9] nt
	s_add_u32 s8, s8, 0x1000
	s_addc_u32 s9, s9, 0
	global_store_dword v15, v33, s[8:9] nt
	s_add_u32 s8, s8, 0x1000
	s_addc_u32 s9, s9, 0
	global_store_dword v15, v34, s[8:9] nt
	s_add_u32 s8, s8, 0x1000
	s_addc_u32 s9, s9, 0
	global_store_dword v15, v35, s[8:9] nt
	s_add_u32 s8, s8, 0x5000
	s_addc_u32 s9, s9, 0
	global_store_dword v15, v36, s[8:9] nt
	s_add_u32 s8, s8, 0x1000
	s_addc_u32 s9, s9, 0
	global_store_dword v15, v37, s[8:9] nt
	s_add_u32 s8, s8, 0x1000
	s_addc_u32 s9, s9, 0
	global_store_dword v15, v38, s[8:9] nt
	s_add_u32 s8, s8, 0x1000
	s_addc_u32 s9, s9, 0
	global_store_dword v15, v39, s[8:9] nt
	s_add_u32 s8, s8, 0x5000
	s_addc_u32 s9, s9, 0
	global_store_dword v15, v40, s[8:9] nt
	s_add_u32 s8, s8, 0x1000
	s_addc_u32 s9, s9, 0
	global_store_dword v15, v41, s[8:9] nt
	s_add_u32 s8, s8, 0x1000
	s_addc_u32 s9, s9, 0
	global_store_dword v15, v42, s[8:9] nt
	s_add_u32 s8, s8, 0x1000
	s_addc_u32 s9, s9, 0
	global_store_dword v15, v43, s[8:9] nt
	s_add_u32 s8, s8, 0x5000
	s_addc_u32 s9, s9, 0
	global_store_dword v15, v44, s[8:9] nt
	s_add_u32 s8, s8, 0x1000
	s_addc_u32 s9, s9, 0
	global_store_dword v15, v45, s[8:9] nt
	s_add_u32 s8, s8, 0x1000
	s_addc_u32 s9, s9, 0
	global_store_dword v15, v46, s[8:9] nt
	s_add_u32 s8, s8, 0x1000
	s_addc_u32 s9, s9, 0
	global_store_dword v15, v47, s[8:9] nt
	s_endpgm
